# code placement: 4-byte pads in cold code so every hot loop head sits at the baseline's byte phase (mod 8)
# speedup vs baseline: 1.0110x; 1.0110x over previous
.LBB0_245:
	s_ashr_i32 s19, s18, 31
	s_lshl_b64 s[30:31], s[18:19], 19
	s_add_u32 s30, s44, s30
	s_addc_u32 s31, s45, s31
	s_and_b64 s[34:35], s[4:5], exec
	s_cselect_b32 s11, s31, s13
	s_cselect_b32 s19, s30, s12
	s_ashr_i32 s29, s28, 31
	s_lshl_b64 s[34:35], s[28:29], 19
	s_add_u32 s34, s46, s34
	s_addc_u32 s35, s47, s35
	s_and_b64 s[36:37], s[4:5], exec
	s_cselect_b32 s29, s35, s15
	s_cselect_b32 s60, s34, s14
	s_add_u32 s61, s14, 0x100
	s_addc_u32 s62, s15, 0
	s_mov_b32 s63, -2
	s_nop 0

.LBB0_353:
	s_lshl_b32 s30, 1, s16
	s_add_u32 s33, s92, 0xa1400000
	s_addc_u32 s78, s93, 0
	s_add_u32 s34, s92, 0x57400000
	s_addc_u32 s35, s93, 0
	s_add_u32 s40, s92, 0x600000
	v_mov_b32_e32 v11, 0
	v_add_lshl_u32 v10, s14, v107, 7
	s_addc_u32 s41, s93, 0
	s_lshl_b32 s16, s22, 4
	v_lshl_add_u64 v[96:97], s[10:11], 0, v[6:7]
	v_lshl_add_u64 v[98:99], s[12:13], 0, v[6:7]
	v_lshl_add_u64 v[6:7], v[4:5], 0, v[10:11]
	v_lshl_add_u64 v[8:9], v[2:3], 0, v[10:11]
	global_load_dwordx4 v[30:33], v[6:7], off
	global_load_dwordx4 v[34:37], v[8:9], off
	v_or_b32_e32 v6, s14, v105
	s_add_u32 s8, s33, s8
	v_and_b32_e32 v46, 15, v0
	v_lshlrev_b32_e32 v10, 7, v6
	s_addc_u32 s9, s78, s9
	s_add_i32 s10, s14, s16
	v_lshl_add_u64 v[4:5], v[4:5], 0, v[10:11]
	v_lshl_add_u64 v[2:3], v[2:3], 0, v[10:11]
	v_or_b32_e32 v10, s10, v46
	v_lshlrev_b32_e32 v47, 1, v0
	global_load_dwordx4 v[38:41], v[4:5], off
	global_load_dwordx4 v[42:45], v[2:3], off
	v_lshlrev_b64 v[2:3], 7, v[10:11]
	v_and_b32_e32 v94, 0x60, v47
	v_mov_b32_e32 v95, v11
	v_lshl_add_u64 v[2:3], s[8:9], 0, v[2:3]
	v_lshl_add_u64 v[2:3], v[2:3], 0, v[94:95]
	global_load_dwordx4 v[6:9], v[2:3], off offset:16
	s_nop 0
	global_load_dwordx4 v[2:5], v[2:3], off
	v_and_b32_e32 v10, 7, v0
	v_or_b32_e32 v108, s16, v46
	v_lshlrev_b32_e32 v46, 1, v10
	v_lshlrev_b32_e32 v10, 4, v10
	v_and_b32_e32 v52, 0x50, v0
	v_xad_u32 v10, v10, v52, 0
	v_lshrrev_b32_e32 v52, 1, v0
	v_bfe_u32 v50, v0, 5, 2
	v_or_b32_e32 v51, 1, v46
	v_and_b32_e32 v53, 4, v52
	v_and_b32_e32 v52, 12, v52
	v_lshlrev_b32_e32 v61, 2, v107
	v_bitop3_b32 v60, v52, v46, v50 bitop3:0x36
	v_bitop3_b32 v52, v52, v51, v50 bitop3:0x36
	s_add_i32 s21, 0, 0x10000
	v_and_b32_e32 v61, 12, v61
	v_lshlrev_b32_e32 v59, 8, v105
	v_lshl_add_u32 v60, v60, 4, s21
	v_lshl_add_u32 v52, v52, 4, s21
	v_bitop3_b32 v62, v61, v46, v50 bitop3:0x36
	v_bitop3_b32 v61, v61, v51, v50 bitop3:0x36
	v_add_u32_e32 v115, v60, v59
	v_add_u32_e32 v116, v52, v59
	v_lshlrev_b32_e32 v59, 8, v107
	v_lshlrev_b32_e32 v62, 4, v62
	v_lshlrev_b32_e32 v61, 4, v61
	v_add3_u32 v118, s21, v62, v59
	v_add3_u32 v119, s21, v61, v59
	v_or_b32_e32 v59, 0x80, v105
	v_lshlrev_b32_e32 v61, 8, v59
	v_add_u32_e32 v122, v52, v61
	v_add_u32_e32 v52, 0x80, v107
	s_movk_i32 s14, 0x1e0
	v_and_b32_e32 v48, 3, v0
	s_and_b32 s17, s22, 0x3fffffe
	v_and_or_b32 v47, v47, 8, v53
	v_lshrrev_b32_e32 v53, 1, v1
	v_and_b32_e32 v54, 4, v105
	v_lshl_add_u32 v114, v105, 7, v10
	v_lshl_add_u32 v117, v107, 7, v10
	v_lshl_add_u32 v120, v59, 7, v10
	v_lshl_add_u32 v123, v52, 7, v10
	v_add3_u32 v10, v0, v13, s14
	s_movk_i32 s14, 0x81
	v_and_or_b32 v53, v53, 8, v54
	v_lshrrev_b32_e32 v54, 3, v1
	s_add_i32 s18, 0, 0x20000
	s_lshl_b32 s19, s17, 4
	v_cmp_gt_u32_e64 s[14:15], s14, v10
	v_or_b32_e32 v10, v47, v48
	v_and_b32_e32 v54, 6, v54
	v_lshl_add_u32 v127, v12, 2, s18
	v_or_b32_e32 v12, s19, v10
	s_sub_i32 s79, 8, s17
	v_or_b32_e32 v55, 1, v54
	v_mov_b32_e32 v57, s18
	s_add_i32 s20, s19, 32
	v_lshl_add_u32 v126, v0, 2, s18
	v_readlane_b32 s18, v254, 8
	v_lshlrev_b32_e32 v128, 7, v12
	v_lshrrev_b32_e32 v12, 1, v10
	s_cmpk_lt_u32 s18, 0x200
	v_bitop3_b32 v13, v12, v54, 5 bitop3:0x6c
	v_bitop3_b32 v12, v12, v55, 5 bitop3:0x6c
	s_cselect_b64 s[46:47], -1, 0
	v_lshlrev_b32_e32 v129, 4, v13
	v_lshlrev_b32_e32 v130, 4, v12
	v_or3_b32 v12, v48, s16, v47
	v_mov_b32_e32 v13, 0x800
	s_cmpk_lt_u32 s18, 0x180
	v_lshl_or_b32 v131, v12, 7, v13
	v_lshrrev_b32_e32 v12, 1, v12
	s_cselect_b64 s[48:49], -1, 0
	s_cmp_lt_u32 s17, 5
	v_bitop3_b32 v13, v12, v54, 5 bitop3:0x6c
	v_bitop3_b32 v12, v12, v55, 5 bitop3:0x6c
	s_cselect_b64 s[50:51], -1, 0
	s_add_i32 s16, s19, 48
	v_lshlrev_b32_e32 v133, 4, v12
	v_or_b32_e32 v12, s20, v10
	s_cmpk_lt_u32 s18, 0x100
	v_lshlrev_b32_e32 v134, 7, v12
	v_or_b32_e32 v12, s16, v10
	s_cselect_b64 s[52:53], -1, 0
	s_add_i32 s16, s19, 64
	s_cmp_lt_u32 s17, 3
	v_sub_u32_e32 v56, 0, v0
	v_lshlrev_b32_e32 v135, 7, v12
	v_or_b32_e32 v12, s16, v10
	s_cselect_b64 s[54:55], -1, 0
	s_add_i32 s16, s19, 0x50
	v_and_b32_e32 v56, 3, v56
	s_movk_i32 s10, 0x350
	s_cmpk_lt_u32 s18, 0x80
	v_mad_u32_u24 v57, v56, s10, v57
	v_add_u32_e32 v56, v108, v56
	v_lshlrev_b32_e32 v136, 7, v12
	v_or_b32_e32 v12, s16, v10
	s_cselect_b64 s[56:57], -1, 0
	s_add_i32 s16, s19, 0x60
	v_sub_u32_e32 v56, s19, v56
	v_lshlrev_b32_e32 v137, 7, v12
	v_or_b32_e32 v12, s16, v10
	s_add_i32 s16, s19, 0x70
	v_bfe_u32 v49, v0, 2, 2
	v_lshlrev_b32_e32 v56, 2, v56
	v_lshlrev_b32_e32 v58, 2, v53
	v_lshlrev_b32_e32 v138, 7, v12
	v_or_b32_e32 v12, s16, v10
	s_add_i32 s16, s19, 0x80
	v_add3_u32 v111, v57, v56, v58
	v_add_u32_e32 v113, 0x290, v57
	v_or3_b32 v49, v53, s19, v49
	v_bfe_u32 v56, v0, 1, 1
	v_and_b32_e32 v57, 12, v0
	v_lshrrev_b32_e32 v53, 2, v53
	v_lshlrev_b32_e32 v139, 7, v12
	v_or_b32_e32 v12, s16, v10
	v_lshlrev_b32_e32 v140, 7, v12
	v_bitop3_b32 v12, v53, v56, v57 bitop3:0x36
	v_lshlrev_b32_e32 v149, 4, v12
	v_or_b32_e32 v12, 2, v56
	v_bitop3_b32 v12, v53, v12, v57 bitop3:0x36
	v_lshlrev_b32_e32 v150, 4, v12
	v_or_b32_e32 v12, 4, v56
	v_bitop3_b32 v12, v53, v12, v57 bitop3:0x36
	v_lshlrev_b32_e32 v151, 4, v12
	v_or_b32_e32 v12, 6, v56
	v_bitop3_b32 v12, v53, v12, v57 bitop3:0x36
	v_lshlrev_b32_e32 v152, 4, v12
	v_or_b32_e32 v12, 8, v56
	v_bitop3_b32 v12, v53, v12, v57 bitop3:0x36
	v_lshlrev_b32_e32 v153, 4, v12
	v_or_b32_e32 v12, 10, v56
	v_bitop3_b32 v12, v53, v12, v57 bitop3:0x36
	v_add_u32_e32 v121, v60, v61
	v_lshlrev_b32_e32 v60, 2, v52
	s_addk_i32 s19, 0x90
	v_lshlrev_b32_e32 v154, 4, v12
	v_or_b32_e32 v12, 12, v56
	v_lshlrev_b32_e32 v58, 3, v0
	v_and_b32_e32 v60, 12, v60
	v_or_b32_e32 v10, s19, v10
	v_bitop3_b32 v12, v53, v12, v57 bitop3:0x36
	v_and_b32_e32 v58, 8, v58
	v_bitop3_b32 v46, v60, v46, v50 bitop3:0x36
	v_bitop3_b32 v50, v60, v51, v50 bitop3:0x36
	v_lshlrev_b32_e32 v141, 7, v10
	v_lshlrev_b32_e32 v10, 8, v49
	v_lshlrev_b32_e32 v155, 4, v12
	v_or_b32_e32 v12, 14, v56
	v_lshlrev_b32_e32 v59, 8, v52
	v_lshlrev_b32_e32 v46, 4, v46
	v_lshlrev_b32_e32 v50, 4, v50
	s_movk_i32 s12, 0x150
	v_bitop3_b32 v12, v53, v12, v57 bitop3:0x36
	v_add3_u32 v157, s21, v10, v58
	v_mbcnt_lo_u32_b32 v10, -1, 0
	v_or_b32_e32 v110, 0xffffff80, v105
	v_add_u32_e32 v112, 0x80, v111
	v_cmp_gt_u32_e64 s[8:9], 16, v1
	v_add3_u32 v124, s21, v46, v59
	v_add3_u32 v125, s21, v50, v59
	v_cmp_gt_u32_e64 s[10:11], s10, v0
	v_cmp_gt_u32_e64 s[12:13], s12, v0
	v_lshlrev_b32_e32 v132, 4, v13
	v_add_u32_e32 v142, 0xc0, v111
	v_add_u32_e32 v143, 0x100, v111
	v_add_u32_e32 v144, 0x140, v111
	v_add_u32_e32 v145, 0x180, v111
	v_add_u32_e32 v146, 0x1c0, v111
	v_add_u32_e32 v147, 0x200, v111
	v_add_u32_e32 v148, 0x240, v111
	v_lshlrev_b32_e32 v156, 4, v12
	v_and_b32_e32 v100, 48, v0
	v_mov_b32_e32 v101, v11
	s_mov_b32 s80, 0x800000
	s_mov_b32 s94, 0x3f317217
	s_mov_b32 s76, 0x7f800000
	s_mov_b32 s77, 0x409b43d5
	s_mov_b32 s36, s31
	s_mov_b32 s37, s31
	s_mov_b32 s38, s31
	s_mov_b32 s39, s31
	v_mbcnt_hi_u32_b32 v158, -1, v10
	v_mov_b32_e32 v159, 0xff800000
	v_mov_b32_e32 v160, 0x41b17218
	s_mov_b32 s81, 0
	s_nop 0
	s_branch .LBB0_355

.LBB0_953:
	s_xor_b64 s[36:37], s[10:11], -1
	v_mov_b32_e32 v68, v67
	v_mov_b32_e32 v69, v67
	v_mov_b32_e32 v211, v67
	v_mov_b32_e32 v209, v67
	s_add_u32 s25, s8, 0x100
	v_mov_b32_e32 v66, v67
	s_addc_u32 s27, s9, 0
	v_lshl_add_u64 v[216:217], s[16:17], 0, v[210:211]
	v_lshl_add_u64 v[218:219], s[16:17], 0, v[208:209]
	s_mov_b32 s61, -2
	s_mov_b64 s[38:39], 0
	v_cndmask_b32_e64 v201, 0, 1, s[36:37]
	s_branch .Lpk6_entry
	s_nop 0

.LBB0_1118:
	s_xor_b64 s[34:35], s[34:35], -1
	v_mov_b32_e32 v68, v66
	v_mov_b32_e32 v69, v66
	s_add_u32 s19, s8, 0x100
	v_mov_b32_e32 v67, v66
	s_addc_u32 s21, s9, 0
	s_mov_b32 s63, -2
	v_cndmask_b32_e64 v242, 0, 1, s[34:35]
	s_branch .Lpk7_entry
	s_nop 0

.LBB0_1202:
	global_load_dword v12, v[2:3], off
	global_load_dword v13, v[4:5], off
	global_load_dword v14, v[6:7], off
	global_load_dword v15, v[8:9], off
	global_load_dword v16, v[2:3], off offset:2048
	global_load_dword v17, v[4:5], off offset:2048
	global_load_dword v18, v[6:7], off offset:2048
	global_load_dword v19, v[8:9], off offset:2048
	s_mov_b64 s[2:3], 0x1000
	v_lshl_add_u64 v[2:3], v[2:3], 0, s[2:3]
	v_lshl_add_u64 v[4:5], v[4:5], 0, s[2:3]
	v_lshl_add_u64 v[6:7], v[6:7], 0, s[2:3]
	v_lshl_add_u64 v[8:9], v[8:9], 0, s[2:3]
	global_load_dword v20, v[2:3], off
	global_load_dword v21, v[4:5], off
	global_load_dword v22, v[6:7], off
	global_load_dword v23, v[8:9], off
	global_load_dword v24, v[2:3], off offset:2048
	global_load_dword v25, v[4:5], off offset:2048
	global_load_dword v26, v[6:7], off offset:2048
	global_load_dword v27, v[8:9], off offset:2048
	s_waitcnt vmcnt(12)
	ds_write2st64_b32 v11, v12, v13 offset1:32
	ds_write2st64_b32 v11, v14, v15 offset0:64 offset1:96
	s_waitcnt vmcnt(8)
	ds_write2st64_b32 v11, v16, v17 offset0:8 offset1:40
	ds_write2st64_b32 v11, v18, v19 offset0:72 offset1:104
	s_waitcnt vmcnt(4)
	ds_write2st64_b32 v11, v20, v21 offset0:16 offset1:48
	ds_write2st64_b32 v11, v22, v23 offset0:80 offset1:112
	s_waitcnt vmcnt(0)
	ds_write2st64_b32 v11, v24, v25 offset0:24 offset1:56
	ds_write2st64_b32 v11, v26, v27 offset0:88 offset1:120
	s_or_b64 exec, exec, s[0:1]
	s_ashr_i32 s97, s96, 31
	s_lshl_b64 s[0:1], s[96:97], 3
	s_add_u32 s4, s0, s86
	s_addc_u32 s5, s1, 0
	v_mov_b64_e32 v[2:3], 0x3fff
	v_cmp_gt_u64_e32 vcc, s[4:5], v[2:3]
	s_mov_b32 s87, 0
	s_mov_b32 s9, 3
	s_waitcnt lgkmcnt(0)
	s_barrier
	s_cbranch_vccnz .LBB0_1206
	s_ashr_i32 s91, s90, 31
	s_lshl_b64 s[6:7], s[90:91], 3
	v_lshrrev_b32_e32 v2, 2, v1
	v_mul_lo_u32 v2, s6, v2
	v_add_lshl_u32 v2, s4, v2, 2
	v_and_b32_e32 v3, 3, v0
	s_mov_b32 s0, 0xfffc
	v_and_or_b32 v2, v2, s0, v3
	v_lshlrev_b32_e32 v96, 2, v2
	v_mov_b32_e32 v97, 0
	v_lshl_add_u64 v[2:3], s[92:93], 0, v[96:97]
	v_add_co_u32_e32 v4, vcc, 0x100000, v2
	s_lshl_b64 s[2:3], s[96:97], 6
	s_nop 0
	v_addc_co_u32_e32 v5, vcc, 0, v3, vcc
	global_load_dword v8, v[4:5], off
	v_add_co_u32_e32 v2, vcc, 0x140000, v2
	s_lshl_b32 s12, s86, 3
	s_nop 0
	v_addc_co_u32_e32 v3, vcc, 0, v3, vcc
	global_load_dword v9, v[2:3], off
	s_add_u32 s21, s2, s12
	v_lshlrev_b32_e32 v4, 4, v0
	v_and_b32_e32 v5, 15, v0
	v_and_b32_e32 v0, 32, v0
	s_addc_u32 s22, s3, 0
	s_lshl_b64 s[12:13], s[90:91], 6
	s_lshl_b64 s[2:3], s[96:97], 15
	s_lshl_b64 s[14:15], s[86:87], 12
	v_lshrrev_b32_e32 v3, 4, v1
	v_lshlrev_b32_e32 v5, 5, v5
	v_lshrrev_b32_e32 v0, 1, v0
	s_add_u32 s2, s2, s14
	v_lshlrev_b32_e32 v10, 9, v3
	v_or3_b32 v0, s2, v5, v0
	s_addc_u32 s24, s3, s15
	v_or_b32_e32 v6, v10, v0
	s_mov_b64 s[18:19], 0x69400000
	s_movk_i32 s23, 0x200
	v_mov_b32_e32 v107, s24
	v_or_b32_e32 v106, 0xc00, v6
	v_lshl_add_u64 v[108:109], v[106:107], 0, s[18:19]
	v_and_or_b32 v106, v10, s23, v0
	s_lshl_b64 s[14:15], s[90:91], 15
	s_lshl_b64 s[2:3], s[96:97], 16
	s_lshl_b64 s[16:17], s[86:87], 13
	v_and_b32_e32 v96, 0xf0, v4
	s_add_u32 s2, s2, s16
	v_lshlrev_b32_e32 v2, 8, v3
	v_mov_b32_e32 v3, v97
	v_lshl_add_u64 v[4:5], s[92:93], 0, v[96:97]
	v_lshlrev_b32_e32 v11, 2, v96
	s_addc_u32 s3, s3, s17
	s_mov_b64 s[0:1], 0x8f400000
	v_or_b32_e32 v6, 0x400, v6
	v_mov_b32_e32 v7, s24
	v_lshl_add_u64 v[2:3], v[4:5], 0, v[2:3]
	v_and_or_b32 v96, v1, 48, v11
	s_add_u32 s16, s74, s2
	v_mov_b32_e32 v126, 0x79400000
	s_mov_b32 s11, 0x69400000
	s_mov_b32 s8, 0x3f9837f0
	s_mov_b32 s10, 0x3d800000
	v_mov_b32_e32 v127, 0x3727c5ac
	s_mov_b32 s20, 0xf800000
	v_mov_b32_e32 v128, 0x260
	v_mov_b32_e32 v99, v97
	v_mov_b32_e32 v101, v97
	v_mov_b32_e32 v103, v97
	v_mov_b32_e32 v105, v97
	v_lshl_add_u64 v[110:111], v[6:7], 0, s[18:19]
	v_lshl_add_u64 v[112:113], v[2:3], 0, s[0:1]
	v_add_u32_e32 v129, 0, v96
	s_addc_u32 s17, s75, s3
	s_lshl_b64 s[18:19], s[90:91], 16
	v_or_b32_e32 v98, 0x1000, v96
	v_or_b32_e32 v100, 0x1400, v96
	v_or_b32_e32 v102, 0x1800, v96
	v_or_b32_e32 v104, 0x1c00, v96
	v_mov_b64_e32 v[114:115], 0x4000
	s_waitcnt vmcnt(1)
	v_lshl_add_u32 v0, v8, 2, 0
	v_add_u32_e32 v0, 0x25100, v0
	ds_read_b32 v0, v0
	s_waitcnt vmcnt(0) lgkmcnt(0)
	v_lshl_add_u32 v130, v0, 8, v9
	s_nop 0
